# P0 x-norm row loop: all 8 row loads hoisted to loop top with counted vmcnt, gain vector preloaded once outside the loop (removes 8 serialized round trips per row); plus in-proj weight prefetch
# speedup vs baseline: 1.0128x; 1.0128x over previous
.LBB0_2191:
	s_cmpk_gt_i32 s14, 0x3fff
	s_cbranch_scc1 .LBB0_2194
	v_add_u32_e32 v1, 64, v12
	v_cmp_lt_i32_e32 vcc, v11, v1
	s_load_dwordx2 s[2:3], s[16:17], 0x0
	s_load_dwordx2 s[4:5], s[16:17], 0x18
	s_waitcnt lgkmcnt(0)
	v_cndmask_b32_e32 v2, v172, v11, vcc
	v_cmp_lt_i32_e32 vcc, v10, v1
	v_lshlrev_b32_e32 v35, 2, v2
	v_lshlrev_b32_e32 v0, 5, v159
	v_cndmask_b32_e32 v2, v172, v10, vcc
	v_cmp_lt_i32_e32 vcc, v9, v1
	v_lshlrev_b32_e32 v36, 2, v2
	s_ashr_i32 s15, s14, 31
	v_cndmask_b32_e32 v2, v172, v9, vcc
	v_cmp_lt_i32_e32 vcc, v8, v1
	v_lshlrev_b32_e32 v37, 2, v2
	s_ashr_i32 s61, s60, 31
	v_cndmask_b32_e32 v2, v172, v8, vcc
	v_cmp_lt_i32_e32 vcc, v7, v1
	v_lshlrev_b32_e32 v38, 2, v2
	s_lshl_b64 s[6:7], s[14:15], 13
	v_cndmask_b32_e32 v2, v172, v7, vcc
	v_cmp_lt_i32_e32 vcc, v6, v1
	v_lshlrev_b32_e32 v39, 2, v2
	v_or_b32_e32 v2, 0x1000, v0
	v_cndmask_b32_e32 v1, v172, v6, vcc
	v_lshlrev_b32_e32 v40, 2, v1
	v_mov_b32_e32 v1, 0
	v_mov_b32_e32 v3, v1
	v_lshl_add_u64 v[18:19], s[4:5], 0, v[2:3]
	v_or_b32_e32 v2, 0x1800, v0
	v_lshl_add_u64 v[16:17], s[4:5], 0, v[0:1]
	v_lshl_add_u64 v[20:21], s[4:5], 0, v[2:3]
	s_lshl_b64 s[4:5], s[14:15], 12
	v_lshl_or_b32 v22, v159, 4, s4
	v_mov_b32_e32 v23, s5
	s_mov_b64 s[4:5], 0x1de00000
	v_lshl_add_u64 v[24:25], v[22:23], 0, s[4:5]
	s_lshl_b64 s[4:5], s[60:61], 12
	s_add_u32 s2, s2, s6
	s_addc_u32 s3, s3, s7
	v_lshl_add_u64 v[0:1], s[2:3], 0, v[0:1]
	s_mov_b64 s[2:3], 0x1000
	v_lshl_add_u64 v[26:27], v[0:1], 0, s[2:3]
	s_lshl_b64 s[2:3], s[14:15], 11
	s_lshl_b64 s[6:7], s[60:61], 13
	v_lshl_or_b32 v28, v159, 3, s2
	v_mov_b32_e32 v29, s3
	s_lshl_b64 s[8:9], s[60:61], 11
	s_mov_b32 s15, 0x15e00000
	v_mov_b32_e32 v41, 0x358637bd
	s_mov_b32 s16, 0x800000
	s_mov_b32 s17, 0xc3e00000
	v_mov_b32_e32 v42, 0x43e00000
	s_mov_b32 s18, 0x38400000
	global_load_dwordx4 v[176:179], v[16:17], off
	global_load_dwordx4 v[180:183], v[16:17], off offset:16
	global_load_dwordx4 v[184:187], v[16:17], off offset:2048
	global_load_dwordx4 v[188:191], v[16:17], off offset:2064
	global_load_dwordx4 v[192:195], v[18:19], off
	global_load_dwordx4 v[196:199], v[18:19], off offset:16
	global_load_dwordx4 v[200:203], v[20:21], off
	global_load_dwordx4 v[204:207], v[20:21], off offset:16
	s_waitcnt vmcnt(0)
.LBB0_2193:
	global_load_dwordx4 v[4:7], v[26:27], off offset:-4096
	global_load_dwordx4 v[0:3], v[26:27], off offset:-4080
	global_load_dwordx4 v[44:47], v[26:27], off offset:-2048
	global_load_dwordx4 v[48:51], v[26:27], off offset:-2032
	global_load_dwordx4 v[52:55], v[26:27], off
	global_load_dwordx4 v[56:59], v[26:27], off offset:16
	global_load_dwordx4 v[208:211], v[26:27], off offset:2048
	global_load_dwordx4 v[212:215], v[26:27], off offset:2064
	v_lshl_add_u64 v[8:9], s[10:11], 0, v[22:23]
	v_lshl_add_u64 v[10:11], s[10:11], 0, v[28:29]
	v_add_co_u32_e32 v64, vcc, s15, v8
	v_add_co_u32_e64 v32, s[2:3], s18, v10
	s_nop 0
	v_addc_co_u32_e32 v65, vcc, 0, v9, vcc
	v_addc_co_u32_e64 v33, s[2:3], 0, v11, s[2:3]
	v_mov_b32_e32 v68, 0
	v_mov_b32_e32 v69, 0
	v_lshl_add_u64 v[30:31], s[10:11], 0, v[24:25]
	s_add_i32 s14, s14, s60
	v_lshl_add_u64 v[24:25], v[24:25], 0, s[4:5]
	v_lshl_add_u64 v[28:29], v[28:29], 0, s[8:9]
	v_lshl_add_u64 v[22:23], v[22:23], 0, s[4:5]
	s_cmpk_lt_i32 s14, 0x4000
	s_waitcnt vmcnt(7)
	v_cvt_pk_bf16_f32 v8, v4, v5
	v_cvt_pk_bf16_f32 v9, v6, v7
	s_waitcnt vmcnt(6)
	v_cvt_pk_bf16_f32 v10, v0, v1
	v_cvt_pk_bf16_f32 v11, v2, v3
	global_store_dwordx4 v[64:65], v[8:11], off
	v_mul_f32_e32 v12, v5, v5
	v_mul_f32_e32 v13, v7, v7
	v_mul_f32_e32 v14, v1, v1
	v_fmac_f32_e32 v12, v4, v4
	v_fmac_f32_e32 v13, v6, v6
	v_mul_f32_e32 v15, v3, v3
	v_fmac_f32_e32 v14, v0, v0
	v_add_f32_e32 v8, v12, v13
	v_fmac_f32_e32 v15, v2, v2
	v_add_f32_e32 v8, v8, v14
	v_add_f32_e32 v12, v15, v8
	s_waitcnt vmcnt(6)
	v_cvt_pk_bf16_f32 v8, v44, v45
	v_cvt_pk_bf16_f32 v9, v46, v47
	s_waitcnt vmcnt(5)
	v_cvt_pk_bf16_f32 v10, v48, v49
	v_cvt_pk_bf16_f32 v11, v50, v51
	global_store_dwordx4 v[64:65], v[8:11], off offset:1024
	v_mul_f32_e32 v13, v45, v45
	v_mul_f32_e32 v14, v47, v47
	v_fmac_f32_e32 v13, v44, v44
	v_mul_f32_e32 v15, v49, v49
	v_fmac_f32_e32 v14, v46, v46
	v_add_f32_e32 v8, v12, v13
	v_mul_f32_e32 v34, v51, v51
	v_fmac_f32_e32 v15, v48, v48
	v_add_f32_e32 v8, v14, v8
	v_fmac_f32_e32 v34, v50, v50
	v_add_f32_e32 v8, v15, v8
	v_add_f32_e32 v34, v34, v8
	s_waitcnt vmcnt(5)
	v_cvt_pk_bf16_f32 v8, v52, v53
	v_cvt_pk_bf16_f32 v9, v54, v55
	s_waitcnt vmcnt(4)
	v_cvt_pk_bf16_f32 v10, v56, v57
	v_cvt_pk_bf16_f32 v11, v58, v59
	global_store_dwordx4 v[64:65], v[8:11], off offset:2048
	v_mul_f32_e32 v43, v53, v53
	v_mul_f32_e32 v60, v55, v55
	v_fmac_f32_e32 v43, v52, v52
	v_mul_f32_e32 v61, v57, v57
	v_fmac_f32_e32 v60, v54, v54
	v_add_f32_e32 v34, v43, v34
	v_mul_f32_e32 v62, v59, v59
	v_fmac_f32_e32 v61, v56, v56
	v_add_f32_e32 v34, v60, v34
	v_fmac_f32_e32 v62, v58, v58
	v_add_f32_e32 v34, v61, v34
	v_add_f32_e32 v34, v62, v34
	v_lshl_add_u64 v[26:27], v[26:27], 0, s[6:7]
	s_waitcnt vmcnt(4)
	v_cvt_pk_bf16_f32 v60, v208, v209
	v_cvt_pk_bf16_f32 v61, v210, v211
	s_waitcnt vmcnt(3)
	v_cvt_pk_bf16_f32 v62, v212, v213
	v_cvt_pk_bf16_f32 v63, v214, v215
	v_pk_mul_f32 v[66:67], v[210:211], v[210:211]
	v_pk_mul_f32 v[70:71], v[208:209], v[208:209]
	global_store_dwordx4 v[64:65], v[60:63], off offset:3072
	v_mov_b32_e32 v76, v66
	v_mov_b32_e32 v77, v70
	v_mov_b32_e32 v70, v67
	v_pk_mul_f32 v[72:73], v[214:215], v[214:215]
	v_pk_mul_f32 v[74:75], v[212:213], v[212:213]
	v_pk_add_f32 v[70:71], v[76:77], v[70:71]
	v_mov_b32_e32 v78, v72
	v_mov_b32_e32 v79, v74
	v_mov_b32_e32 v74, v73
	v_add_f32_e32 v34, v71, v34
	v_pk_add_f32 v[72:73], v[78:79], v[74:75]
	v_add_f32_e32 v34, v70, v34
	v_add_f32_e32 v34, v73, v34
	v_add_f32_e32 v34, v72, v34
	ds_bpermute_b32 v43, v35, v34
	s_waitcnt lgkmcnt(0)
	v_add_f32_e32 v34, v34, v43
	ds_bpermute_b32 v43, v36, v34
	s_waitcnt lgkmcnt(0)
	v_add_f32_e32 v34, v34, v43
	ds_bpermute_b32 v43, v37, v34
	s_waitcnt lgkmcnt(0)
	v_add_f32_e32 v34, v34, v43
	ds_bpermute_b32 v43, v38, v34
	s_waitcnt lgkmcnt(0)
	v_add_f32_e32 v34, v34, v43
	ds_bpermute_b32 v43, v39, v34
	s_waitcnt lgkmcnt(0)
	v_add_f32_e32 v34, v34, v43
	ds_bpermute_b32 v43, v40, v34
	s_waitcnt lgkmcnt(0)
	v_add_f32_e32 v34, v34, v43
	v_fmamk_f32 v34, v34, 0x3a000000, v41
	v_mul_f32_e32 v43, 0x4b800000, v34
	v_cmp_gt_f32_e32 vcc, s16, v34
	s_nop 1
	v_cndmask_b32_e32 v34, v34, v43, vcc
	v_rsq_f32_e32 v34, v34
	s_nop 0
	v_mul_f32_e32 v43, 0x45800000, v34
	v_cndmask_b32_e32 v34, v34, v43, vcc
	v_pk_mul_f32 v[4:5], v[4:5], v[34:35] op_sel_hi:[1,0]
	v_pk_mul_f32 v[0:1], v[0:1], v[34:35] op_sel_hi:[1,0]
	v_pk_mul_f32 v[6:7], v[6:7], v[34:35] op_sel_hi:[1,0]
	v_pk_mul_f32 v[2:3], v[2:3], v[34:35] op_sel_hi:[1,0]
	v_pk_mul_f32 v[44:45], v[44:45], v[34:35] op_sel_hi:[1,0]
	v_pk_mul_f32 v[48:49], v[48:49], v[34:35] op_sel_hi:[1,0]
	v_pk_mul_f32 v[46:47], v[46:47], v[34:35] op_sel_hi:[1,0]
	v_pk_mul_f32 v[50:51], v[50:51], v[34:35] op_sel_hi:[1,0]
	v_pk_mul_f32 v[208:209], v[208:209], v[34:35] op_sel_hi:[1,0]
	v_pk_mul_f32 v[212:213], v[212:213], v[34:35] op_sel_hi:[1,0]
	v_pk_mul_f32 v[210:211], v[210:211], v[34:35] op_sel_hi:[1,0]
	v_pk_mul_f32 v[214:215], v[214:215], v[34:35] op_sel_hi:[1,0]
	v_pk_mul_f32 v[4:5], v[176:177], v[4:5]
	v_pk_mul_f32 v[60:61], v[180:181], v[0:1]
	v_pk_mul_f32 v[6:7], v[178:179], v[6:7]
	v_pk_mul_f32 v[62:63], v[182:183], v[2:3]
	v_mul_f32_e32 v43, 0x42000000, v4
	v_mul_f32_e32 v64, 0x42000000, v5
	v_mul_f32_e32 v67, 0x42000000, v60
	v_mul_f32_e32 v70, 0x42000000, v61
	v_cvt_pk_bf16_f32 v0, v4, v5
	v_cvt_pk_bf16_f32 v2, v60, v61
	v_med3_f32 v4, v43, s17, v42
	v_med3_f32 v5, v64, s17, v42
	v_med3_f32 v43, v67, s17, v42
	v_med3_f32 v60, v70, s17, v42
	v_cvt_pk_fp8_f32 v68, v4, v5
	v_cvt_pk_fp8_f32 v69, v43, v60
	v_mul_f32_e32 v65, 0x42000000, v6
	v_mul_f32_e32 v66, 0x42000000, v7
	v_mul_f32_e32 v71, 0x42000000, v62
	v_mul_f32_e32 v72, 0x42000000, v63
	v_cvt_pk_bf16_f32 v1, v6, v7
	v_cvt_pk_bf16_f32 v3, v62, v63
	v_med3_f32 v6, v65, s17, v42
	v_med3_f32 v7, v66, s17, v42
	v_med3_f32 v61, v71, s17, v42
	v_med3_f32 v62, v72, s17, v42
	v_cvt_pk_fp8_f32 v68, v6, v7 op_sel:[0,0,1]
	v_cvt_pk_fp8_f32 v69, v61, v62 op_sel:[0,0,1]
	global_store_dwordx2 v[32:33], v[68:69], off
	global_store_dwordx4 v[30:31], v[0:3], off
	v_mov_b32_e32 v60, 0
	v_mov_b32_e32 v61, 0
	v_pk_mul_f32 v[0:1], v[184:185], v[44:45]
	v_pk_mul_f32 v[4:5], v[188:189], v[48:49]
	v_pk_mul_f32 v[2:3], v[186:187], v[46:47]
	v_mul_f32_e32 v43, 0x42000000, v0
	v_mul_f32_e32 v44, 0x42000000, v1
	v_mul_f32_e32 v47, 0x42000000, v4
	v_mul_f32_e32 v48, 0x42000000, v5
	v_mul_f32_e32 v45, 0x42000000, v2
	v_cvt_pk_bf16_f32 v0, v0, v1
	v_cvt_pk_bf16_f32 v1, v2, v3
	v_cvt_pk_bf16_f32 v2, v4, v5
	v_med3_f32 v4, v43, s17, v42
	v_med3_f32 v5, v44, s17, v42
	v_med3_f32 v43, v47, s17, v42
	v_med3_f32 v44, v48, s17, v42
	v_cvt_pk_fp8_f32 v60, v4, v5
	v_cvt_pk_fp8_f32 v61, v43, v44
	v_pk_mul_f32 v[6:7], v[190:191], v[50:51]
	v_mul_f32_e32 v46, 0x42000000, v3
	v_mul_f32_e32 v49, 0x42000000, v6
	v_mul_f32_e32 v50, 0x42000000, v7
	v_cvt_pk_bf16_f32 v3, v6, v7
	v_med3_f32 v6, v45, s17, v42
	v_med3_f32 v7, v46, s17, v42
	v_med3_f32 v45, v49, s17, v42
	v_med3_f32 v46, v50, s17, v42
	v_cvt_pk_fp8_f32 v60, v6, v7 op_sel:[0,0,1]
	v_cvt_pk_fp8_f32 v61, v45, v46 op_sel:[0,0,1]
	global_store_dwordx2 v[32:33], v[60:61], off offset:512
	global_store_dwordx4 v[30:31], v[0:3], off offset:1024
	v_pk_mul_f32 v[46:47], v[52:53], v[34:35] op_sel_hi:[1,0]
	v_pk_mul_f32 v[48:49], v[56:57], v[34:35] op_sel_hi:[1,0]
	v_pk_mul_f32 v[50:51], v[54:55], v[34:35] op_sel_hi:[1,0]
	v_mov_b32_e32 v44, 0
	v_mov_b32_e32 v45, 0
	v_pk_mul_f32 v[52:53], v[58:59], v[34:35] op_sel_hi:[1,0]
	v_pk_mul_f32 v[0:1], v[46:47], v[192:193]
	v_pk_mul_f32 v[4:5], v[48:49], v[196:197]
	v_pk_mul_f32 v[2:3], v[50:51], v[194:195]
	v_mul_f32_e32 v43, 0x42000000, v0
	v_mul_f32_e32 v46, 0x42000000, v1
	v_mul_f32_e32 v49, 0x42000000, v4
	v_mul_f32_e32 v50, 0x42000000, v5
	v_mul_f32_e32 v47, 0x42000000, v2
	v_cvt_pk_bf16_f32 v0, v0, v1
	v_cvt_pk_bf16_f32 v1, v2, v3
	v_cvt_pk_bf16_f32 v2, v4, v5
	v_med3_f32 v4, v43, s17, v42
	v_med3_f32 v5, v46, s17, v42
	v_med3_f32 v43, v49, s17, v42
	v_med3_f32 v46, v50, s17, v42
	v_cvt_pk_fp8_f32 v44, v4, v5
	v_cvt_pk_fp8_f32 v45, v43, v46
	v_pk_mul_f32 v[6:7], v[52:53], v[198:199]
	v_mul_f32_e32 v48, 0x42000000, v3
	v_mul_f32_e32 v51, 0x42000000, v6
	v_mul_f32_e32 v52, 0x42000000, v7
	v_cvt_pk_bf16_f32 v3, v6, v7
	v_med3_f32 v6, v47, s17, v42
	v_med3_f32 v7, v48, s17, v42
	v_med3_f32 v47, v51, s17, v42
	v_med3_f32 v48, v52, s17, v42
	v_cvt_pk_fp8_f32 v44, v6, v7 op_sel:[0,0,1]
	v_cvt_pk_fp8_f32 v45, v47, v48 op_sel:[0,0,1]
	global_store_dwordx2 v[32:33], v[44:45], off offset:1024
	global_store_dwordx4 v[30:31], v[0:3], off offset:2048
	v_mov_b32_e32 v44, 0
	v_mov_b32_e32 v45, 0
	v_pk_mul_f32 v[0:1], v[208:209], v[200:201]
	v_pk_mul_f32 v[4:5], v[212:213], v[204:205]
	v_pk_mul_f32 v[2:3], v[210:211], v[202:203]
	v_pk_mul_f32 v[6:7], v[214:215], v[206:207]
	v_mul_f32_e32 v8, 0x42000000, v0
	v_mul_f32_e32 v9, 0x42000000, v1
	v_mul_f32_e32 v10, 0x42000000, v2
	v_mul_f32_e32 v11, 0x42000000, v3
	v_mul_f32_e32 v12, 0x42000000, v4
	v_mul_f32_e32 v13, 0x42000000, v5
	v_cvt_pk_bf16_f32 v0, v0, v1
	v_cvt_pk_bf16_f32 v1, v2, v3
	v_med3_f32 v2, v8, s17, v42
	v_med3_f32 v3, v9, s17, v42
	v_med3_f32 v8, v10, s17, v42
	v_med3_f32 v9, v11, s17, v42
	v_med3_f32 v10, v12, s17, v42
	v_med3_f32 v11, v13, s17, v42
	v_cvt_pk_fp8_f32 v44, v2, v3
	v_cvt_pk_fp8_f32 v45, v10, v11
	v_mul_f32_e32 v14, 0x42000000, v6
	v_mul_f32_e32 v15, 0x42000000, v7
	v_med3_f32 v12, v14, s17, v42
	v_med3_f32 v2, v15, s17, v42
	v_cvt_pk_fp8_f32 v44, v8, v9 op_sel:[0,0,1]
	v_cvt_pk_fp8_f32 v45, v12, v2 op_sel:[0,0,1]
	v_cvt_pk_bf16_f32 v2, v4, v5
	v_cvt_pk_bf16_f32 v3, v6, v7
	global_store_dwordx2 v[32:33], v[44:45], off offset:1536
	global_store_dwordx4 v[30:31], v[0:3], off offset:3072
	s_cbranch_scc1 .LBB0_2193
